# baseline (speedup 1.0000x reference)
.LBB2_6:
	s_or_b64 exec, exec, s[18:19]
	v_xor_b32_e32 v23, 32, v23
	s_add_i32 s38, 0, 0x1c000
	v_lshlrev_b32_e32 v23, 2, v23
	v_lshlrev_b32_e32 v199, 2, v25
	s_waitcnt vmcnt(4) lgkmcnt(0)
	s_barrier
	v_add3_u32 v23, s38, v23, v199
	ds_read_b32 v23, v23
	v_max_f32_e32 v24, v24, v24
	v_mul_f32_e32 v22, 0x3db8aa3b, v22
	v_mov_b32_e32 v164, 0
	v_mov_b32_e32 v165, 0
	s_waitcnt lgkmcnt(0)
	s_movk_i32 s45, 0x4000
	v_add3_u32 v234, s45, v184, v185
	v_add3_u32 v235, s45, v184, v186
	v_add3_u32 v236, s45, v184, v187
	v_add3_u32 v237, s45, v184, v188
	ds_read_b128 v[218:221], v234 offset:49152
	ds_read_b128 v[222:225], v235 offset:49152
	ds_read_b128 v[226:229], v236 offset:49152
	ds_read_b128 v[230:233], v237 offset:49152
	v_add3_u32 v234, s45, v184, v189
	v_add3_u32 v235, s45, v184, v190
	v_add3_u32 v236, s45, v184, v191
	v_add3_u32 v237, s45, v184, v192
	ds_read_b128 v[202:205], v234 offset:49152
	ds_read_b128 v[206:209], v235 offset:49152
	ds_read_b128 v[210:213], v236 offset:49152
	ds_read_b128 v[214:217], v237 offset:49152
	v_max_f32_e32 v23, v23, v23
	v_max_f32_e32 v197, v24, v23
	v_mov_b32_e32 v23, 2.0
	v_fmamk_f32 v200, v197, 0xbdb8aa3b, v23
	v_fmamk_f32 v23, v22, 0xcb400000, v200
	v_fma_f32 v2, v2, v22, v23
	v_fma_f32 v3, v3, v22, v23
	v_fma_f32 v6, v6, v22, v23
	v_fma_f32 v7, v7, v22, v23
	v_fma_f32 v10, v10, v22, v23
	v_fma_f32 v11, v11, v22, v23
	v_fma_f32 v14, v14, v22, v23
	v_fma_f32 v15, v15, v22, v23
	v_exp_f32_e32 v2, v2
	v_exp_f32_e32 v3, v3
	v_exp_f32_e32 v6, v6
	v_exp_f32_e32 v7, v7
	v_exp_f32_e32 v10, v10
	v_exp_f32_e32 v11, v11
	v_exp_f32_e32 v14, v14
	v_exp_f32_e32 v15, v15
	v_fma_f32 v4, v4, v22, v23
	v_fma_f32 v5, v5, v22, v23
	v_fma_f32 v8, v8, v22, v23
	v_fma_f32 v9, v9, v22, v23
	v_fma_f32 v12, v12, v22, v23
	v_fma_f32 v13, v13, v22, v23
	v_fma_f32 v16, v16, v22, v23
	v_fmac_f32_e32 v23, v17, v22
	v_mov_b32_e32 v166, 0
	v_mov_b32_e32 v167, 0
	v_exp_f32_e32 v4, v4
	v_exp_f32_e32 v5, v5
	v_exp_f32_e32 v8, v8
	v_exp_f32_e32 v9, v9
	v_exp_f32_e32 v12, v12
	v_exp_f32_e32 v13, v13
	v_exp_f32_e32 v16, v16
	v_exp_f32_e32 v17, v23
	v_add_f32_e32 v234, v2, v3
	v_add_f32_e32 v235, v4, v5
	v_add_f32_e32 v236, v6, v7
	v_add_f32_e32 v237, v8, v9
	v_add_f32_e32 v234, v234, v235
	v_add_f32_e32 v236, v236, v237
	v_add_f32_e32 v235, v10, v11
	v_add_f32_e32 v237, v12, v13
	v_add_f32_e32 v234, v234, v236
	v_add_f32_e32 v235, v235, v237
	v_add_f32_e32 v236, v14, v15
	v_add_f32_e32 v237, v16, v17
	v_add_f32_e32 v234, v234, v235
	v_add_f32_e32 v236, v236, v237
	v_add_f32_e32 v234, v234, v236
	v_cvt_pk_fp8_f32 v164, v2, v3
	v_cvt_pk_fp8_f32 v165, v6, v7
	v_cvt_pk_fp8_f32 v166, v10, v11
	v_cvt_pk_fp8_f32 v167, v14, v15
	s_lshl_b32 s0, s22, 11
	s_add_i32 s0, s0, 0
	s_add_i32 s0, s0, 0x18000
	v_cvt_pk_fp8_f32 v164, v4, v5 op_sel:[0,0,1]
	v_cvt_pk_fp8_f32 v165, v8, v9 op_sel:[0,0,1]
	v_cvt_pk_fp8_f32 v166, v12, v13 op_sel:[0,0,1]
	v_cvt_pk_fp8_f32 v167, v16, v17 op_sel:[0,0,1]
	v_lshl_add_u32 v193, v198, 4, s0
	v_lshrrev_b32_e32 v3, 2, v0
	v_lshlrev_b32_e32 v6, 1, v183
	s_lshl_b32 s0, s20, 20
	v_bfe_u32 v4, v0, 2, 2
	v_lshl_or_b32 v5, v1, 6, s24
	v_bitop3_b32 v3, v6, v3, 3 bitop3:0x78
	s_or_b32 s18, s0, s23
	v_lshl_add_u32 v194, s34, 10, v193
	v_lshl_or_b32 v195, v3, 4, v5
	v_bitop3_b32 v3, v6, v4, 1 bitop3:0x36
	v_add3_u32 v4, s21, v20, v21
	s_add_u32 s0, s6, s18
	ds_write_b128 v194, v[164:167]
	v_lshl_or_b32 v196, v3, 4, v5
	v_ashrrev_i32_e32 v5, 31, v4
	s_addc_u32 s1, s7, 0
	s_waitcnt vmcnt(2) lgkmcnt(0)
	s_barrier
	s_mov_b64 s[60:61], s[0:1]
	v_lshl_add_u64 v[170:171], s[0:1], 0, v[4:5]
	v_add3_u32 v4, s21, v18, v19
	s_add_u32 s0, s8, s18
	v_mov_b32_e32 v2, 0
	v_ashrrev_i32_e32 v5, 31, v4
	s_addc_u32 s1, s9, 0
	s_mov_b32 s39, 0
	s_mov_b32 s40, 1
	s_mov_b64 s[64:65], s[0:1]
	v_lshl_add_u64 v[172:173], s[0:1], 0, v[4:5]
	s_mov_b64 s[6:7], 0
	s_movk_i32 s41, 0x2000
	s_mov_b64 s[8:9], 0xc000
	s_mov_b64 s[18:19], 0xe000
	s_mov_b64 s[20:21], 0x8000
	s_mov_b64 s[22:23], 0xa000
	s_mov_b32 s42, 0x42966666
	v_mov_b32_e32 v82, 0x4b400000
	v_mov_b32_e32 v100, 0x38383838
	s_mov_b32 s0, 0
	s_mov_b32 s43, 1
	v_mov_b32_e32 v3, v2
	v_mov_b32_e32 v4, v2
	v_mov_b32_e32 v5, v2
	v_mov_b32_e32 v6, v2
	v_mov_b32_e32 v7, v2
	v_mov_b32_e32 v8, v2
	v_mov_b32_e32 v9, v2
	v_mov_b32_e32 v10, v2
	v_mov_b32_e32 v11, v2
	v_mov_b32_e32 v12, v2
	v_mov_b32_e32 v13, v2
	v_mov_b32_e32 v14, v2
	v_mov_b32_e32 v15, v2
	v_mov_b32_e32 v16, v2
	v_mov_b32_e32 v17, v2
	v_mov_b32_e32 v18, v2
	v_mov_b32_e32 v19, v2
	v_mov_b32_e32 v20, v2
	v_mov_b32_e32 v21, v2
	v_mov_b32_e32 v22, v2
	v_mov_b32_e32 v23, v2
	v_mov_b32_e32 v24, v2
	v_mov_b32_e32 v25, v2
	v_mov_b32_e32 v26, v2
	v_mov_b32_e32 v27, v2
	v_mov_b32_e32 v28, v2
	v_mov_b32_e32 v29, v2
	v_mov_b32_e32 v30, v2
	v_mov_b32_e32 v31, v2
	v_mov_b32_e32 v32, v2
	v_mov_b32_e32 v33, v2
	v_mov_b32_e32 v34, v2
	v_mov_b32_e32 v35, v2
	v_mov_b32_e32 v36, v2
	v_mov_b32_e32 v37, v2
	v_mov_b32_e32 v38, v2
	v_mov_b32_e32 v39, v2
	v_mov_b32_e32 v40, v2
	v_mov_b32_e32 v41, v2
	v_mov_b32_e32 v42, v2
	v_mov_b32_e32 v43, v2
	v_mov_b32_e32 v44, v2
	v_mov_b32_e32 v45, v2
	v_mov_b32_e32 v46, v2
	v_mov_b32_e32 v47, v2
	v_mov_b32_e32 v48, v2
	v_mov_b32_e32 v49, v2
	v_mov_b32_e32 v50, v2
	v_mov_b32_e32 v51, v2
	v_mov_b32_e32 v52, v2
	v_mov_b32_e32 v53, v2
	v_mov_b32_e32 v54, v2
	v_mov_b32_e32 v55, v2
	v_mov_b32_e32 v56, v2
	v_mov_b32_e32 v57, v2
	v_mov_b32_e32 v58, v2
	v_mov_b32_e32 v59, v2
	v_mov_b32_e32 v60, v2
	v_mov_b32_e32 v61, v2
	v_mov_b32_e32 v62, v2
	v_mov_b32_e32 v63, v2
	v_mov_b32_e32 v64, v2
	v_mov_b32_e32 v65, v2
	v_mov_b32_e32 v66, v2
	v_mov_b32_e32 v67, v2
	v_mov_b32_e32 v68, v2
	v_mov_b32_e32 v69, v2
	v_mov_b32_e32 v70, v2
	v_mov_b32_e32 v71, v2
	v_mov_b32_e32 v72, v2
	v_mov_b32_e32 v73, v2
	v_mov_b32_e32 v74, v2
	v_mov_b32_e32 v75, v2
	v_mov_b32_e32 v76, v2
	v_mov_b32_e32 v77, v2
	v_mov_b32_e32 v78, v2
	v_mov_b32_e32 v79, v2
	v_mov_b32_e32 v80, v2
	v_mov_b32_e32 v81, v2
	v_mov_b32_e32 v100, v234
	v_mov_b32_e32 v66, 0x4b400000
	v_mov_b32_e32 v67, v66
	v_mov_b32_e32 v68, v66
	v_mov_b32_e32 v69, v66
	v_mov_b32_e32 v70, v66
	v_mov_b32_e32 v71, v66
	v_mov_b32_e32 v72, v66
	v_mov_b32_e32 v73, v66
	v_mov_b32_e32 v74, v66
	v_mov_b32_e32 v75, v66
	v_mov_b32_e32 v76, v66
	v_mov_b32_e32 v77, v66
	v_mov_b32_e32 v78, v66
	v_mov_b32_e32 v79, v66
	v_mov_b32_e32 v80, v66
	v_mov_b32_e32 v81, v66
	v_add_u32_e32 v234, 0xc000, v184
	v_add_u32_e32 v185, v185, v234
	v_add_u32_e32 v186, v186, v234
	v_add_u32_e32 v187, v187, v234
	v_add_u32_e32 v188, v188, v234
	v_add_u32_e32 v189, v189, v234
	v_add_u32_e32 v190, v190, v234
	v_add_u32_e32 v191, v191, v234
	v_add_u32_e32 v192, v192, v234
	v_subrev_u32_e32 v236, s60, v170
	v_subrev_u32_e32 v239, s64, v172
	s_sub_u32 s1, s64, s60
	s_add_i32 s1, s1, 0xffffc000
	v_add_u32_e32 v238, 0x2000, v236
	v_add_u32_e32 v239, s1, v239
	v_add_u32_e32 v201, 0x2000, v239
	s_add_u32 s60, s60, 0xc000
	s_addc_u32 s61, s61, 0
	s_mov_b32 s42, 0x43dc0000
	s_mov_b64 s[54:55], -1
	v_accvgpr_write_b32 a0, v34
	v_accvgpr_write_b32 a1, v35
	v_accvgpr_write_b32 a2, v36
	v_accvgpr_write_b32 a3, v37
	v_accvgpr_write_b32 a4, v38
	v_accvgpr_write_b32 a5, v39
	v_accvgpr_write_b32 a6, v40
	v_accvgpr_write_b32 a7, v41
	v_accvgpr_write_b32 a8, v42
	v_accvgpr_write_b32 a9, v43
	v_accvgpr_write_b32 a10, v44
	v_accvgpr_write_b32 a11, v45
	v_accvgpr_write_b32 a12, v46
	v_accvgpr_write_b32 a13, v47
	v_accvgpr_write_b32 a14, v48
	v_accvgpr_write_b32 a15, v49
	v_mfma_i32_32x32x32_i8 v[84:99], v[218:221], v[132:135], v[66:81]
	v_mfma_i32_32x32x32_i8 v[84:99], v[222:225], v[136:139], v[84:99]
.Lat_u0:
	ds_read_b128 v[108:111], v193
	ds_read_b128 v[112:115], v193 offset:1024
	v_mfma_i32_32x32x32_i8 v[84:99], v[226:229], v[140:143], v[84:99]
	ds_read_b128 v[116:119], v195 offset:6144
	ds_read_b128 v[120:123], v196 offset:6144
	s_cmp_gt_u32 s43, 29
	s_cbranch_scc1 .Lat_nok0
	s_add_i32 m0, s31, 49152
	ds_read_b128 v[124:127], v195 offset:4096
	global_load_lds_dwordx4 v236, s[60:61]
	s_add_i32 m0, s31, 57344
	v_mfma_i32_32x32x32_i8 v[84:99], v[230:233], v[144:147], v[84:99]
	global_load_lds_dwordx4 v238, s[60:61]
	s_branch .Lat_k0
.Lat_nok0:
	ds_read_b128 v[124:127], v195 offset:4096
	v_mfma_i32_32x32x32_i8 v[84:99], v[230:233], v[144:147], v[84:99]
.Lat_k0:
	ds_read_b128 v[128:131], v196 offset:4096
	v_mfma_i32_32x32x32_i8 v[84:99], v[202:205], v[148:151], v[84:99]
	ds_read_b128 v[202:205], v195
	v_mfma_i32_32x32x32_i8 v[84:99], v[206:209], v[152:155], v[84:99]
	ds_read_b128 v[206:209], v196
	v_mfma_i32_32x32x32_i8 v[84:99], v[210:213], v[156:159], v[84:99]
	ds_read_b128 v[210:213], v195 offset:2048
	v_mfma_i32_32x32x32_i8 v[84:99], v[214:217], v[160:163], v[84:99]
	ds_read_b128 v[214:217], v196 offset:2048
	v_readlane_b32 s50, v182, s43
	s_waitcnt lgkmcnt(6)
	v_mfma_f32_32x32x64_f8f6f4 v[2:17], v[108:115], v[116:123], v[2:17]
	ds_read_b128 v[218:221], v185 offset:32768
	ds_read_b128 v[222:225], v186 offset:32768
	ds_read_b128 v[226:229], v187 offset:32768
	ds_read_b128 v[230:233], v188 offset:32768
	v_mul_f32_e32 v82, s50, v168
	v_mul_f32_e32 v234, 0x3db8aa3b, v82
	v_fmamk_f32 v235, v234, 0xcb400000, v200
	s_cmp_gt_u32 s43, 30
	s_cbranch_scc1 .Lat_nov0
	s_add_i32 m0, s31, 32768
	v_fma_f32 v84, v84, v234, v235
	global_load_lds_dwordx4 v239, s[60:61]
	s_add_i32 m0, s31, 40960
	v_fma_f32 v85, v85, v234, v235
	global_load_lds_dwordx4 v201, s[60:61]
	s_branch .Lat_v0
.Lat_nov0:
	v_fma_f32 v84, v84, v234, v235
	v_fma_f32 v85, v85, v234, v235
.Lat_v0:
	v_fma_f32 v86, v86, v234, v235
	v_fma_f32 v87, v87, v234, v235
	v_exp_f32_e32 v84, v84
	v_exp_f32_e32 v85, v85
	v_exp_f32_e32 v86, v86
	v_exp_f32_e32 v87, v87
	v_fma_f32 v88, v88, v234, v235
	v_fma_f32 v89, v89, v234, v235
	v_fma_f32 v90, v90, v234, v235
	v_fma_f32 v91, v91, v234, v235
	s_waitcnt lgkmcnt(8)
	v_mfma_f32_32x32x64_f8f6f4 v[18:33], v[108:115], v[124:131], v[18:33]
	v_add_f32_e32 v101, v84, v85
	v_add_f32_e32 v102, v86, v87
	v_exp_f32_e32 v88, v88
	v_exp_f32_e32 v89, v89
	v_exp_f32_e32 v90, v90
	v_exp_f32_e32 v91, v91
	v_add_f32_e32 v101, v101, v102
	v_cvt_pk_fp8_f32 v164, v84, v85
	v_cvt_pk_fp8_f32 v164, v86, v87 op_sel:[0,0,1]
	v_fma_f32 v92, v92, v234, v235
	v_fma_f32 v93, v93, v234, v235
	v_fma_f32 v94, v94, v234, v235
	v_fma_f32 v95, v95, v234, v235
	v_add_f32_e32 v102, v88, v89
	v_add_f32_e32 v103, v90, v91
	s_waitcnt lgkmcnt(6)
	v_mfma_f32_32x32x64_f8f6f4 v[50:65], v[108:115], v[202:209], v[50:65]
	ds_read_b128 v[202:205], v189 offset:32768
	ds_read_b128 v[206:209], v190 offset:32768
	v_exp_f32_e32 v92, v92
	v_exp_f32_e32 v93, v93
	v_exp_f32_e32 v94, v94
	v_exp_f32_e32 v95, v95
	v_add_f32_e32 v102, v102, v103
	v_cvt_pk_fp8_f32 v165, v88, v89
	v_cvt_pk_fp8_f32 v165, v90, v91 op_sel:[0,0,1]
	v_fma_f32 v96, v96, v234, v235
	v_fma_f32 v97, v97, v234, v235
	v_fma_f32 v98, v98, v234, v235
	v_fma_f32 v99, v99, v234, v235
	v_add_f32_e32 v101, v101, v102
	v_add_f32_e32 v102, v92, v93
	v_add_f32_e32 v103, v94, v95
	s_waitcnt lgkmcnt(6)
	v_mfma_f32_32x32x64_f8f6f4 a[0:15], v[108:115], v[210:217], a[0:15]
	ds_read_b128 v[210:213], v191 offset:32768
	ds_read_b128 v[214:217], v192 offset:32768
	v_exp_f32_e32 v96, v96
	v_exp_f32_e32 v97, v97
	v_exp_f32_e32 v98, v98
	v_exp_f32_e32 v99, v99
	v_add_f32_e32 v102, v102, v103
	v_cvt_pk_fp8_f32 v166, v92, v93
	v_cvt_pk_fp8_f32 v166, v94, v95 op_sel:[0,0,1]
	v_add_f32_e32 v101, v101, v102
	v_add_f32_e32 v102, v96, v97
	v_add_f32_e32 v103, v98, v99
	s_add_u32 s60, s60, 0x4000
	s_addc_u32 s61, s61, 0
	v_add_f32_e32 v102, v102, v103
	v_cvt_pk_fp8_f32 v167, v96, v97
	v_cvt_pk_fp8_f32 v167, v98, v99 op_sel:[0,0,1]
	v_add_f32_e32 v101, v101, v102
	ds_write_b128 v194, v[164:167] offset:8192
	v_cmp_ge_f32_e64 s[52:53], s42, v101
	v_add_f32_e32 v100, v100, v101
	s_add_i32 s43, s43, 1
	s_nop 0
	s_and_b64 s[54:55], s[54:55], s[52:53]
	s_cmp_eq_u32 s43, 32
	s_cbranch_scc1 .Lat_last
	s_waitcnt lgkmcnt(7)
	v_mfma_i32_32x32x32_i8 v[84:99], v[218:221], v[132:135], v[66:81]
	v_mfma_i32_32x32x32_i8 v[84:99], v[222:225], v[136:139], v[84:99]
	s_waitcnt vmcnt(2) lgkmcnt(0)
	s_barrier
.Lat_u1:
	ds_read_b128 v[108:111], v193 offset:8192
	ds_read_b128 v[112:115], v193 offset:9216
	v_mfma_i32_32x32x32_i8 v[84:99], v[226:229], v[140:143], v[84:99]
	ds_read_b128 v[116:119], v195 offset:22528
	ds_read_b128 v[120:123], v196 offset:22528
	s_add_i32 m0, s31, 65536
	ds_read_b128 v[124:127], v195 offset:20480
	global_load_lds_dwordx4 v236, s[60:61]
	s_add_i32 m0, s31, 73728
	v_mfma_i32_32x32x32_i8 v[84:99], v[230:233], v[144:147], v[84:99]
	global_load_lds_dwordx4 v238, s[60:61]
	ds_read_b128 v[128:131], v196 offset:20480
	v_mfma_i32_32x32x32_i8 v[84:99], v[202:205], v[148:151], v[84:99]
	ds_read_b128 v[202:205], v195 offset:16384
	v_mfma_i32_32x32x32_i8 v[84:99], v[206:209], v[152:155], v[84:99]
	ds_read_b128 v[206:209], v196 offset:16384
	v_mfma_i32_32x32x32_i8 v[84:99], v[210:213], v[156:159], v[84:99]
	ds_read_b128 v[210:213], v195 offset:18432
	v_mfma_i32_32x32x32_i8 v[84:99], v[214:217], v[160:163], v[84:99]
	ds_read_b128 v[214:217], v196 offset:18432
	v_readlane_b32 s50, v182, s43
	s_waitcnt lgkmcnt(6)
	v_mfma_f32_32x32x64_f8f6f4 v[2:17], v[108:115], v[116:123], v[2:17]
	ds_read_b128 v[218:221], v185
	ds_read_b128 v[222:225], v186
	ds_read_b128 v[226:229], v187
	ds_read_b128 v[230:233], v188
	v_mul_f32_e32 v82, s50, v168
	v_mul_f32_e32 v234, 0x3db8aa3b, v82
	v_fmamk_f32 v235, v234, 0xcb400000, v200
	s_mov_b32 m0, s31
	v_fma_f32 v84, v84, v234, v235
	global_load_lds_dwordx4 v239, s[60:61]
	s_add_i32 m0, s31, 8192
	v_fma_f32 v85, v85, v234, v235
	global_load_lds_dwordx4 v201, s[60:61]
	v_fma_f32 v86, v86, v234, v235
	v_fma_f32 v87, v87, v234, v235
	v_exp_f32_e32 v84, v84
	v_exp_f32_e32 v85, v85
	v_exp_f32_e32 v86, v86
	v_exp_f32_e32 v87, v87
	v_fma_f32 v88, v88, v234, v235
	v_fma_f32 v89, v89, v234, v235
	v_fma_f32 v90, v90, v234, v235
	v_fma_f32 v91, v91, v234, v235
	s_waitcnt lgkmcnt(8)
	v_mfma_f32_32x32x64_f8f6f4 v[18:33], v[108:115], v[124:131], v[18:33]
	v_add_f32_e32 v101, v84, v85
	v_add_f32_e32 v102, v86, v87
	v_exp_f32_e32 v88, v88
	v_exp_f32_e32 v89, v89
	v_exp_f32_e32 v90, v90
	v_exp_f32_e32 v91, v91
	v_add_f32_e32 v101, v101, v102
	v_cvt_pk_fp8_f32 v164, v84, v85
	v_cvt_pk_fp8_f32 v164, v86, v87 op_sel:[0,0,1]
	v_fma_f32 v92, v92, v234, v235
	v_fma_f32 v93, v93, v234, v235
	v_fma_f32 v94, v94, v234, v235
	v_fma_f32 v95, v95, v234, v235
	v_add_f32_e32 v102, v88, v89
	v_add_f32_e32 v103, v90, v91
	s_waitcnt lgkmcnt(6)
	v_mfma_f32_32x32x64_f8f6f4 v[50:65], v[108:115], v[202:209], v[50:65]
	ds_read_b128 v[202:205], v189
	ds_read_b128 v[206:209], v190
	v_exp_f32_e32 v92, v92
	v_exp_f32_e32 v93, v93
	v_exp_f32_e32 v94, v94
	v_exp_f32_e32 v95, v95
	v_add_f32_e32 v102, v102, v103
	v_cvt_pk_fp8_f32 v165, v88, v89
	v_cvt_pk_fp8_f32 v165, v90, v91 op_sel:[0,0,1]
	v_fma_f32 v96, v96, v234, v235
	v_fma_f32 v97, v97, v234, v235
	v_fma_f32 v98, v98, v234, v235
	v_fma_f32 v99, v99, v234, v235
	v_add_f32_e32 v101, v101, v102
	v_add_f32_e32 v102, v92, v93
	v_add_f32_e32 v103, v94, v95
	s_waitcnt lgkmcnt(6)
	v_mfma_f32_32x32x64_f8f6f4 a[0:15], v[108:115], v[210:217], a[0:15]
	ds_read_b128 v[210:213], v191
	ds_read_b128 v[214:217], v192
	v_exp_f32_e32 v96, v96
	v_exp_f32_e32 v97, v97
	v_exp_f32_e32 v98, v98
	v_exp_f32_e32 v99, v99
	v_add_f32_e32 v102, v102, v103
	v_cvt_pk_fp8_f32 v166, v92, v93
	v_cvt_pk_fp8_f32 v166, v94, v95 op_sel:[0,0,1]
	v_add_f32_e32 v101, v101, v102
	v_add_f32_e32 v102, v96, v97
	v_add_f32_e32 v103, v98, v99
	s_add_u32 s60, s60, 0x4000
	s_addc_u32 s61, s61, 0
	v_add_f32_e32 v102, v102, v103
	v_cvt_pk_fp8_f32 v167, v96, v97
	v_cvt_pk_fp8_f32 v167, v98, v99 op_sel:[0,0,1]
	v_add_f32_e32 v101, v101, v102
	ds_write_b128 v194, v[164:167]
	v_cmp_ge_f32_e64 s[52:53], s42, v101
	v_add_f32_e32 v100, v100, v101
	s_add_i32 s43, s43, 1
	s_nop 0
	s_and_b64 s[54:55], s[54:55], s[52:53]
	s_waitcnt lgkmcnt(7)
	v_mfma_i32_32x32x32_i8 v[84:99], v[218:221], v[132:135], v[66:81]
	v_mfma_i32_32x32x32_i8 v[84:99], v[222:225], v[136:139], v[84:99]
	s_waitcnt vmcnt(2) lgkmcnt(0)
	s_barrier
.Lat_u2:
	ds_read_b128 v[108:111], v193
	ds_read_b128 v[112:115], v193 offset:1024
	v_mfma_i32_32x32x32_i8 v[84:99], v[226:229], v[140:143], v[84:99]
	ds_read_b128 v[116:119], v195 offset:38912
	ds_read_b128 v[120:123], v196 offset:38912
	s_add_i32 m0, s31, 81920
	ds_read_b128 v[124:127], v195 offset:36864
	global_load_lds_dwordx4 v236, s[60:61]
	s_add_i32 m0, s31, 90112
	v_mfma_i32_32x32x32_i8 v[84:99], v[230:233], v[144:147], v[84:99]
	global_load_lds_dwordx4 v238, s[60:61]
	ds_read_b128 v[128:131], v196 offset:36864
	v_mfma_i32_32x32x32_i8 v[84:99], v[202:205], v[148:151], v[84:99]
	ds_read_b128 v[202:205], v195 offset:32768
	v_mfma_i32_32x32x32_i8 v[84:99], v[206:209], v[152:155], v[84:99]
	ds_read_b128 v[206:209], v196 offset:32768
	v_mfma_i32_32x32x32_i8 v[84:99], v[210:213], v[156:159], v[84:99]
	ds_read_b128 v[210:213], v195 offset:34816
	v_mfma_i32_32x32x32_i8 v[84:99], v[214:217], v[160:163], v[84:99]
	ds_read_b128 v[214:217], v196 offset:34816
	v_readlane_b32 s50, v182, s43
	s_waitcnt lgkmcnt(6)
	v_mfma_f32_32x32x64_f8f6f4 v[2:17], v[108:115], v[116:123], v[2:17]
	ds_read_b128 v[218:221], v185 offset:16384
	ds_read_b128 v[222:225], v186 offset:16384
	ds_read_b128 v[226:229], v187 offset:16384
	ds_read_b128 v[230:233], v188 offset:16384
	v_mul_f32_e32 v82, s50, v168
	v_mul_f32_e32 v234, 0x3db8aa3b, v82
	v_fmamk_f32 v235, v234, 0xcb400000, v200
	s_add_i32 m0, s31, 16384
	v_fma_f32 v84, v84, v234, v235
	global_load_lds_dwordx4 v239, s[60:61]
	s_add_i32 m0, s31, 24576
	v_fma_f32 v85, v85, v234, v235
	global_load_lds_dwordx4 v201, s[60:61]
	v_fma_f32 v86, v86, v234, v235
	v_fma_f32 v87, v87, v234, v235
	v_exp_f32_e32 v84, v84
	v_exp_f32_e32 v85, v85
	v_exp_f32_e32 v86, v86
	v_exp_f32_e32 v87, v87
	v_fma_f32 v88, v88, v234, v235
	v_fma_f32 v89, v89, v234, v235
	v_fma_f32 v90, v90, v234, v235
	v_fma_f32 v91, v91, v234, v235
	s_waitcnt lgkmcnt(8)
	v_mfma_f32_32x32x64_f8f6f4 v[18:33], v[108:115], v[124:131], v[18:33]
	v_add_f32_e32 v101, v84, v85
	v_add_f32_e32 v102, v86, v87
	v_exp_f32_e32 v88, v88
	v_exp_f32_e32 v89, v89
	v_exp_f32_e32 v90, v90
	v_exp_f32_e32 v91, v91
	v_add_f32_e32 v101, v101, v102
	v_cvt_pk_fp8_f32 v164, v84, v85
	v_cvt_pk_fp8_f32 v164, v86, v87 op_sel:[0,0,1]
	v_fma_f32 v92, v92, v234, v235
	v_fma_f32 v93, v93, v234, v235
	v_fma_f32 v94, v94, v234, v235
	v_fma_f32 v95, v95, v234, v235
	v_add_f32_e32 v102, v88, v89
	v_add_f32_e32 v103, v90, v91
	s_waitcnt lgkmcnt(6)
	v_mfma_f32_32x32x64_f8f6f4 v[50:65], v[108:115], v[202:209], v[50:65]
	ds_read_b128 v[202:205], v189 offset:16384
	ds_read_b128 v[206:209], v190 offset:16384
	v_exp_f32_e32 v92, v92
	v_exp_f32_e32 v93, v93
	v_exp_f32_e32 v94, v94
	v_exp_f32_e32 v95, v95
	v_add_f32_e32 v102, v102, v103
	v_cvt_pk_fp8_f32 v165, v88, v89
	v_cvt_pk_fp8_f32 v165, v90, v91 op_sel:[0,0,1]
	v_fma_f32 v96, v96, v234, v235
	v_fma_f32 v97, v97, v234, v235
	v_fma_f32 v98, v98, v234, v235
	v_fma_f32 v99, v99, v234, v235
	v_add_f32_e32 v101, v101, v102
	v_add_f32_e32 v102, v92, v93
	v_add_f32_e32 v103, v94, v95
	s_waitcnt lgkmcnt(6)
	v_mfma_f32_32x32x64_f8f6f4 a[0:15], v[108:115], v[210:217], a[0:15]
	ds_read_b128 v[210:213], v191 offset:16384
	ds_read_b128 v[214:217], v192 offset:16384
	v_exp_f32_e32 v96, v96
	v_exp_f32_e32 v97, v97
	v_exp_f32_e32 v98, v98
	v_exp_f32_e32 v99, v99
	v_add_f32_e32 v102, v102, v103
	v_cvt_pk_fp8_f32 v166, v92, v93
	v_cvt_pk_fp8_f32 v166, v94, v95 op_sel:[0,0,1]
	v_add_f32_e32 v101, v101, v102
	v_add_f32_e32 v102, v96, v97
	v_add_f32_e32 v103, v98, v99
	s_add_u32 s60, s60, 0x4000
	s_addc_u32 s61, s61, 0
	v_add_f32_e32 v102, v102, v103
	v_cvt_pk_fp8_f32 v167, v96, v97
	v_cvt_pk_fp8_f32 v167, v98, v99 op_sel:[0,0,1]
	v_add_f32_e32 v101, v101, v102
	ds_write_b128 v194, v[164:167] offset:8192
	v_cmp_ge_f32_e64 s[52:53], s42, v101
	v_add_f32_e32 v100, v100, v101
	s_add_i32 s43, s43, 1
	s_nop 0
	s_and_b64 s[54:55], s[54:55], s[52:53]
	s_waitcnt lgkmcnt(7)
	v_mfma_i32_32x32x32_i8 v[84:99], v[218:221], v[132:135], v[66:81]
	v_mfma_i32_32x32x32_i8 v[84:99], v[222:225], v[136:139], v[84:99]
	s_waitcnt vmcnt(2) lgkmcnt(0)
	s_barrier
.Lat_u3:
	ds_read_b128 v[108:111], v193 offset:8192
	ds_read_b128 v[112:115], v193 offset:9216
	v_mfma_i32_32x32x32_i8 v[84:99], v[226:229], v[140:143], v[84:99]
	ds_read_b128 v[116:119], v195 offset:6144
	ds_read_b128 v[120:123], v196 offset:6144
	s_add_i32 m0, s31, 49152
	ds_read_b128 v[124:127], v195 offset:4096
	global_load_lds_dwordx4 v236, s[60:61]
	s_add_i32 m0, s31, 57344
	v_mfma_i32_32x32x32_i8 v[84:99], v[230:233], v[144:147], v[84:99]
	global_load_lds_dwordx4 v238, s[60:61]
	ds_read_b128 v[128:131], v196 offset:4096
	v_mfma_i32_32x32x32_i8 v[84:99], v[202:205], v[148:151], v[84:99]
	ds_read_b128 v[202:205], v195
	v_mfma_i32_32x32x32_i8 v[84:99], v[206:209], v[152:155], v[84:99]
	ds_read_b128 v[206:209], v196
	v_mfma_i32_32x32x32_i8 v[84:99], v[210:213], v[156:159], v[84:99]
	ds_read_b128 v[210:213], v195 offset:2048
	v_mfma_i32_32x32x32_i8 v[84:99], v[214:217], v[160:163], v[84:99]
	ds_read_b128 v[214:217], v196 offset:2048
	v_readlane_b32 s50, v182, s43
	s_waitcnt lgkmcnt(6)
	v_mfma_f32_32x32x64_f8f6f4 v[2:17], v[108:115], v[116:123], v[2:17]
	ds_read_b128 v[218:221], v185 offset:32768
	ds_read_b128 v[222:225], v186 offset:32768
	ds_read_b128 v[226:229], v187 offset:32768
	ds_read_b128 v[230:233], v188 offset:32768
	v_mul_f32_e32 v82, s50, v168
	v_mul_f32_e32 v234, 0x3db8aa3b, v82
	v_fmamk_f32 v235, v234, 0xcb400000, v200
	s_add_i32 m0, s31, 32768
	v_fma_f32 v84, v84, v234, v235
	global_load_lds_dwordx4 v239, s[60:61]
	s_add_i32 m0, s31, 40960
	v_fma_f32 v85, v85, v234, v235
	global_load_lds_dwordx4 v201, s[60:61]
	v_fma_f32 v86, v86, v234, v235
	v_fma_f32 v87, v87, v234, v235
	v_exp_f32_e32 v84, v84
	v_exp_f32_e32 v85, v85
	v_exp_f32_e32 v86, v86
	v_exp_f32_e32 v87, v87
	v_fma_f32 v88, v88, v234, v235
	v_fma_f32 v89, v89, v234, v235
	v_fma_f32 v90, v90, v234, v235
	v_fma_f32 v91, v91, v234, v235
	s_waitcnt lgkmcnt(8)
	v_mfma_f32_32x32x64_f8f6f4 v[18:33], v[108:115], v[124:131], v[18:33]
	v_add_f32_e32 v101, v84, v85
	v_add_f32_e32 v102, v86, v87
	v_exp_f32_e32 v88, v88
	v_exp_f32_e32 v89, v89
	v_exp_f32_e32 v90, v90
	v_exp_f32_e32 v91, v91
	v_add_f32_e32 v101, v101, v102
	v_cvt_pk_fp8_f32 v164, v84, v85
	v_cvt_pk_fp8_f32 v164, v86, v87 op_sel:[0,0,1]
	v_fma_f32 v92, v92, v234, v235
	v_fma_f32 v93, v93, v234, v235
	v_fma_f32 v94, v94, v234, v235
	v_fma_f32 v95, v95, v234, v235
	v_add_f32_e32 v102, v88, v89
	v_add_f32_e32 v103, v90, v91
	s_waitcnt lgkmcnt(6)
	v_mfma_f32_32x32x64_f8f6f4 v[50:65], v[108:115], v[202:209], v[50:65]
	ds_read_b128 v[202:205], v189 offset:32768
	ds_read_b128 v[206:209], v190 offset:32768
	v_exp_f32_e32 v92, v92
	v_exp_f32_e32 v93, v93
	v_exp_f32_e32 v94, v94
	v_exp_f32_e32 v95, v95
	v_add_f32_e32 v102, v102, v103
	v_cvt_pk_fp8_f32 v165, v88, v89
	v_cvt_pk_fp8_f32 v165, v90, v91 op_sel:[0,0,1]
	v_fma_f32 v96, v96, v234, v235
	v_fma_f32 v97, v97, v234, v235
	v_fma_f32 v98, v98, v234, v235
	v_fma_f32 v99, v99, v234, v235
	v_add_f32_e32 v101, v101, v102
	v_add_f32_e32 v102, v92, v93
	v_add_f32_e32 v103, v94, v95
	s_waitcnt lgkmcnt(6)
	v_mfma_f32_32x32x64_f8f6f4 a[0:15], v[108:115], v[210:217], a[0:15]
	ds_read_b128 v[210:213], v191 offset:32768
	ds_read_b128 v[214:217], v192 offset:32768
	v_exp_f32_e32 v96, v96
	v_exp_f32_e32 v97, v97
	v_exp_f32_e32 v98, v98
	v_exp_f32_e32 v99, v99
	v_add_f32_e32 v102, v102, v103
	v_cvt_pk_fp8_f32 v166, v92, v93
	v_cvt_pk_fp8_f32 v166, v94, v95 op_sel:[0,0,1]
	v_add_f32_e32 v101, v101, v102
	v_add_f32_e32 v102, v96, v97
	v_add_f32_e32 v103, v98, v99
	s_add_u32 s60, s60, 0x4000
	s_addc_u32 s61, s61, 0
	v_add_f32_e32 v102, v102, v103
	v_cvt_pk_fp8_f32 v167, v96, v97
	v_cvt_pk_fp8_f32 v167, v98, v99 op_sel:[0,0,1]
	v_add_f32_e32 v101, v101, v102
	ds_write_b128 v194, v[164:167]
	v_cmp_ge_f32_e64 s[52:53], s42, v101
	v_add_f32_e32 v100, v100, v101
	s_add_i32 s43, s43, 1
	s_nop 0
	s_and_b64 s[54:55], s[54:55], s[52:53]
	s_waitcnt lgkmcnt(7)
	v_mfma_i32_32x32x32_i8 v[84:99], v[218:221], v[132:135], v[66:81]
	v_mfma_i32_32x32x32_i8 v[84:99], v[222:225], v[136:139], v[84:99]
	s_waitcnt vmcnt(2) lgkmcnt(0)
	s_barrier
.Lat_u4:
	ds_read_b128 v[108:111], v193
	ds_read_b128 v[112:115], v193 offset:1024
	v_mfma_i32_32x32x32_i8 v[84:99], v[226:229], v[140:143], v[84:99]
	ds_read_b128 v[116:119], v195 offset:22528
	ds_read_b128 v[120:123], v196 offset:22528
	s_add_i32 m0, s31, 65536
	ds_read_b128 v[124:127], v195 offset:20480
	global_load_lds_dwordx4 v236, s[60:61]
	s_add_i32 m0, s31, 73728
	v_mfma_i32_32x32x32_i8 v[84:99], v[230:233], v[144:147], v[84:99]
	global_load_lds_dwordx4 v238, s[60:61]
	ds_read_b128 v[128:131], v196 offset:20480
	v_mfma_i32_32x32x32_i8 v[84:99], v[202:205], v[148:151], v[84:99]
	ds_read_b128 v[202:205], v195 offset:16384
	v_mfma_i32_32x32x32_i8 v[84:99], v[206:209], v[152:155], v[84:99]
	ds_read_b128 v[206:209], v196 offset:16384
	v_mfma_i32_32x32x32_i8 v[84:99], v[210:213], v[156:159], v[84:99]
	ds_read_b128 v[210:213], v195 offset:18432
	v_mfma_i32_32x32x32_i8 v[84:99], v[214:217], v[160:163], v[84:99]
	ds_read_b128 v[214:217], v196 offset:18432
	v_readlane_b32 s50, v182, s43
	s_waitcnt lgkmcnt(6)
	v_mfma_f32_32x32x64_f8f6f4 v[2:17], v[108:115], v[116:123], v[2:17]
	ds_read_b128 v[218:221], v185
	ds_read_b128 v[222:225], v186
	ds_read_b128 v[226:229], v187
	ds_read_b128 v[230:233], v188
	v_mul_f32_e32 v82, s50, v168
	v_mul_f32_e32 v234, 0x3db8aa3b, v82
	v_fmamk_f32 v235, v234, 0xcb400000, v200
	s_mov_b32 m0, s31
	v_fma_f32 v84, v84, v234, v235
	global_load_lds_dwordx4 v239, s[60:61]
	s_add_i32 m0, s31, 8192
	v_fma_f32 v85, v85, v234, v235
	global_load_lds_dwordx4 v201, s[60:61]
	v_fma_f32 v86, v86, v234, v235
	v_fma_f32 v87, v87, v234, v235
	v_exp_f32_e32 v84, v84
	v_exp_f32_e32 v85, v85
	v_exp_f32_e32 v86, v86
	v_exp_f32_e32 v87, v87
	v_fma_f32 v88, v88, v234, v235
	v_fma_f32 v89, v89, v234, v235
	v_fma_f32 v90, v90, v234, v235
	v_fma_f32 v91, v91, v234, v235
	s_waitcnt lgkmcnt(8)
	v_mfma_f32_32x32x64_f8f6f4 v[18:33], v[108:115], v[124:131], v[18:33]
	v_add_f32_e32 v101, v84, v85
	v_add_f32_e32 v102, v86, v87
	v_exp_f32_e32 v88, v88
	v_exp_f32_e32 v89, v89
	v_exp_f32_e32 v90, v90
	v_exp_f32_e32 v91, v91
	v_add_f32_e32 v101, v101, v102
	v_cvt_pk_fp8_f32 v164, v84, v85
	v_cvt_pk_fp8_f32 v164, v86, v87 op_sel:[0,0,1]
	v_fma_f32 v92, v92, v234, v235
	v_fma_f32 v93, v93, v234, v235
	v_fma_f32 v94, v94, v234, v235
	v_fma_f32 v95, v95, v234, v235
	v_add_f32_e32 v102, v88, v89
	v_add_f32_e32 v103, v90, v91
	s_waitcnt lgkmcnt(6)
	v_mfma_f32_32x32x64_f8f6f4 v[50:65], v[108:115], v[202:209], v[50:65]
	ds_read_b128 v[202:205], v189
	ds_read_b128 v[206:209], v190
	v_exp_f32_e32 v92, v92
	v_exp_f32_e32 v93, v93
	v_exp_f32_e32 v94, v94
	v_exp_f32_e32 v95, v95
	v_add_f32_e32 v102, v102, v103
	v_cvt_pk_fp8_f32 v165, v88, v89
	v_cvt_pk_fp8_f32 v165, v90, v91 op_sel:[0,0,1]
	v_fma_f32 v96, v96, v234, v235
	v_fma_f32 v97, v97, v234, v235
	v_fma_f32 v98, v98, v234, v235
	v_fma_f32 v99, v99, v234, v235
	v_add_f32_e32 v101, v101, v102
	v_add_f32_e32 v102, v92, v93
	v_add_f32_e32 v103, v94, v95
	s_waitcnt lgkmcnt(6)
	v_mfma_f32_32x32x64_f8f6f4 a[0:15], v[108:115], v[210:217], a[0:15]
	ds_read_b128 v[210:213], v191
	ds_read_b128 v[214:217], v192
	v_exp_f32_e32 v96, v96
	v_exp_f32_e32 v97, v97
	v_exp_f32_e32 v98, v98
	v_exp_f32_e32 v99, v99
	v_add_f32_e32 v102, v102, v103
	v_cvt_pk_fp8_f32 v166, v92, v93
	v_cvt_pk_fp8_f32 v166, v94, v95 op_sel:[0,0,1]
	v_add_f32_e32 v101, v101, v102
	v_add_f32_e32 v102, v96, v97
	v_add_f32_e32 v103, v98, v99
	s_add_u32 s60, s60, 0x4000
	s_addc_u32 s61, s61, 0
	v_add_f32_e32 v102, v102, v103
	v_cvt_pk_fp8_f32 v167, v96, v97
	v_cvt_pk_fp8_f32 v167, v98, v99 op_sel:[0,0,1]
	v_add_f32_e32 v101, v101, v102
	ds_write_b128 v194, v[164:167] offset:8192
	v_cmp_ge_f32_e64 s[52:53], s42, v101
	v_add_f32_e32 v100, v100, v101
	s_add_i32 s43, s43, 1
	s_nop 0
	s_and_b64 s[54:55], s[54:55], s[52:53]
	s_waitcnt lgkmcnt(7)
	v_mfma_i32_32x32x32_i8 v[84:99], v[218:221], v[132:135], v[66:81]
	v_mfma_i32_32x32x32_i8 v[84:99], v[222:225], v[136:139], v[84:99]
	s_waitcnt vmcnt(2) lgkmcnt(0)
	s_barrier
.Lat_u5:
	ds_read_b128 v[108:111], v193 offset:8192
	ds_read_b128 v[112:115], v193 offset:9216
	v_mfma_i32_32x32x32_i8 v[84:99], v[226:229], v[140:143], v[84:99]
	ds_read_b128 v[116:119], v195 offset:38912
	ds_read_b128 v[120:123], v196 offset:38912
	s_cmp_gt_u32 s43, 29
	s_cbranch_scc1 .Lat_nok5
	s_add_i32 m0, s31, 81920
	ds_read_b128 v[124:127], v195 offset:36864
	global_load_lds_dwordx4 v236, s[60:61]
	s_add_i32 m0, s31, 90112
	v_mfma_i32_32x32x32_i8 v[84:99], v[230:233], v[144:147], v[84:99]
	global_load_lds_dwordx4 v238, s[60:61]
	s_branch .Lat_k5
.Lat_nok5:
	ds_read_b128 v[124:127], v195 offset:36864
	v_mfma_i32_32x32x32_i8 v[84:99], v[230:233], v[144:147], v[84:99]
.Lat_k5:
	ds_read_b128 v[128:131], v196 offset:36864
	v_mfma_i32_32x32x32_i8 v[84:99], v[202:205], v[148:151], v[84:99]
	ds_read_b128 v[202:205], v195 offset:32768
	v_mfma_i32_32x32x32_i8 v[84:99], v[206:209], v[152:155], v[84:99]
	ds_read_b128 v[206:209], v196 offset:32768
	v_mfma_i32_32x32x32_i8 v[84:99], v[210:213], v[156:159], v[84:99]
	ds_read_b128 v[210:213], v195 offset:34816
	v_mfma_i32_32x32x32_i8 v[84:99], v[214:217], v[160:163], v[84:99]
	ds_read_b128 v[214:217], v196 offset:34816
	v_readlane_b32 s50, v182, s43
	s_waitcnt lgkmcnt(6)
	v_mfma_f32_32x32x64_f8f6f4 v[2:17], v[108:115], v[116:123], v[2:17]
	ds_read_b128 v[218:221], v185 offset:16384
	ds_read_b128 v[222:225], v186 offset:16384
	ds_read_b128 v[226:229], v187 offset:16384
	ds_read_b128 v[230:233], v188 offset:16384
	v_mul_f32_e32 v82, s50, v168
	v_mul_f32_e32 v234, 0x3db8aa3b, v82
	v_fmamk_f32 v235, v234, 0xcb400000, v200
	s_add_i32 m0, s31, 16384
	v_fma_f32 v84, v84, v234, v235
	global_load_lds_dwordx4 v239, s[60:61]
	s_add_i32 m0, s31, 24576
	v_fma_f32 v85, v85, v234, v235
	global_load_lds_dwordx4 v201, s[60:61]
	v_fma_f32 v86, v86, v234, v235
	v_fma_f32 v87, v87, v234, v235
	v_exp_f32_e32 v84, v84
	v_exp_f32_e32 v85, v85
	v_exp_f32_e32 v86, v86
	v_exp_f32_e32 v87, v87
	v_fma_f32 v88, v88, v234, v235
	v_fma_f32 v89, v89, v234, v235
	v_fma_f32 v90, v90, v234, v235
	v_fma_f32 v91, v91, v234, v235
	s_waitcnt lgkmcnt(8)
	v_mfma_f32_32x32x64_f8f6f4 v[18:33], v[108:115], v[124:131], v[18:33]
	v_add_f32_e32 v101, v84, v85
	v_add_f32_e32 v102, v86, v87
	v_exp_f32_e32 v88, v88
	v_exp_f32_e32 v89, v89
	v_exp_f32_e32 v90, v90
	v_exp_f32_e32 v91, v91
	v_add_f32_e32 v101, v101, v102
	v_cvt_pk_fp8_f32 v164, v84, v85
	v_cvt_pk_fp8_f32 v164, v86, v87 op_sel:[0,0,1]
	v_fma_f32 v92, v92, v234, v235
	v_fma_f32 v93, v93, v234, v235
	v_fma_f32 v94, v94, v234, v235
	v_fma_f32 v95, v95, v234, v235
	v_add_f32_e32 v102, v88, v89
	v_add_f32_e32 v103, v90, v91
	s_waitcnt lgkmcnt(6)
	v_mfma_f32_32x32x64_f8f6f4 v[50:65], v[108:115], v[202:209], v[50:65]
	ds_read_b128 v[202:205], v189 offset:16384
	ds_read_b128 v[206:209], v190 offset:16384
	v_exp_f32_e32 v92, v92
	v_exp_f32_e32 v93, v93
	v_exp_f32_e32 v94, v94
	v_exp_f32_e32 v95, v95
	v_add_f32_e32 v102, v102, v103
	v_cvt_pk_fp8_f32 v165, v88, v89
	v_cvt_pk_fp8_f32 v165, v90, v91 op_sel:[0,0,1]
	v_fma_f32 v96, v96, v234, v235
	v_fma_f32 v97, v97, v234, v235
	v_fma_f32 v98, v98, v234, v235
	v_fma_f32 v99, v99, v234, v235
	v_add_f32_e32 v101, v101, v102
	v_add_f32_e32 v102, v92, v93
	v_add_f32_e32 v103, v94, v95
	s_waitcnt lgkmcnt(6)
	v_mfma_f32_32x32x64_f8f6f4 a[0:15], v[108:115], v[210:217], a[0:15]
	ds_read_b128 v[210:213], v191 offset:16384
	ds_read_b128 v[214:217], v192 offset:16384
	v_exp_f32_e32 v96, v96
	v_exp_f32_e32 v97, v97
	v_exp_f32_e32 v98, v98
	v_exp_f32_e32 v99, v99
	v_add_f32_e32 v102, v102, v103
	v_cvt_pk_fp8_f32 v166, v92, v93
	v_cvt_pk_fp8_f32 v166, v94, v95 op_sel:[0,0,1]
	v_add_f32_e32 v101, v101, v102
	v_add_f32_e32 v102, v96, v97
	v_add_f32_e32 v103, v98, v99
	s_add_u32 s60, s60, 0x4000
	s_addc_u32 s61, s61, 0
	v_add_f32_e32 v102, v102, v103
	v_cvt_pk_fp8_f32 v167, v96, v97
	v_cvt_pk_fp8_f32 v167, v98, v99 op_sel:[0,0,1]
	v_add_f32_e32 v101, v101, v102
	ds_write_b128 v194, v[164:167]
	v_cmp_ge_f32_e64 s[52:53], s42, v101
	v_add_f32_e32 v100, v100, v101
	s_add_i32 s43, s43, 1
	s_nop 0
	s_and_b64 s[54:55], s[54:55], s[52:53]
	s_waitcnt lgkmcnt(7)
	v_mfma_i32_32x32x32_i8 v[84:99], v[218:221], v[132:135], v[66:81]
	v_mfma_i32_32x32x32_i8 v[84:99], v[222:225], v[136:139], v[84:99]
	s_cmp_gt_u32 s43, 30
	s_cbranch_scc1 .Lat_drain
	s_waitcnt vmcnt(2) lgkmcnt(0)
	s_barrier
	s_branch .Lat_u0

.Lat_last:
	s_waitcnt vmcnt(0) lgkmcnt(0)
	s_barrier
	s_nop 7
	s_nop 7
	s_nop 7
	v_accvgpr_read_b32 v34, a0
	v_accvgpr_read_b32 v35, a1
	v_accvgpr_read_b32 v36, a2
	v_accvgpr_read_b32 v37, a3
	v_accvgpr_read_b32 v38, a4
	v_accvgpr_read_b32 v39, a5
	v_accvgpr_read_b32 v40, a6
	v_accvgpr_read_b32 v41, a7
	v_accvgpr_read_b32 v42, a8
	v_accvgpr_read_b32 v43, a9
	v_accvgpr_read_b32 v44, a10
	v_accvgpr_read_b32 v45, a11
	v_accvgpr_read_b32 v46, a12
	v_accvgpr_read_b32 v47, a13
	v_accvgpr_read_b32 v48, a14
	v_accvgpr_read_b32 v49, a15
	v_mov_b32_e32 v66, v100
	s_cmp_lg_u64 s[54:55], exec
	s_cselect_b32 s1, 1, 0
	s_or_b32 s39, s39, s1
	v_add_u32_e32 v234, 0xc000, v184
	v_sub_u32_e32 v185, v185, v234
	v_sub_u32_e32 v186, v186, v234
	v_sub_u32_e32 v187, v187, v234
	v_sub_u32_e32 v188, v188, v234
	v_sub_u32_e32 v189, v189, v234
	v_sub_u32_e32 v190, v190, v234
	v_sub_u32_e32 v191, v191, v234
	v_sub_u32_e32 v192, v192, v234

	.amdhsa_kernel _Z11attn_kernelPKhS0_S0_PKfS2_PhPfS4_
		.amdhsa_group_segment_fixed_size 0
		.amdhsa_private_segment_fixed_size 0
		.amdhsa_kernarg_size 64
		.amdhsa_user_sgpr_count 2
		.amdhsa_user_sgpr_dispatch_ptr 0
		.amdhsa_user_sgpr_queue_ptr 0
		.amdhsa_user_sgpr_kernarg_segment_ptr 1
		.amdhsa_user_sgpr_dispatch_id 0
		.amdhsa_user_sgpr_kernarg_preload_length 0
		.amdhsa_user_sgpr_kernarg_preload_offset 0
		.amdhsa_user_sgpr_private_segment_size 0
		.amdhsa_uses_dynamic_stack 0
		.amdhsa_enable_private_segment 0
		.amdhsa_system_sgpr_workgroup_id_x 1
		.amdhsa_system_sgpr_workgroup_id_y 0
		.amdhsa_system_sgpr_workgroup_id_z 0
		.amdhsa_system_sgpr_workgroup_info 0
		.amdhsa_system_vgpr_workitem_id 0
		.amdhsa_next_free_vgpr 256
		.amdhsa_next_free_sgpr 66
		.amdhsa_accum_offset 240
		.amdhsa_reserve_vcc 1
		.amdhsa_float_round_mode_32 0
		.amdhsa_float_round_mode_16_64 0
		.amdhsa_float_denorm_mode_32 3
		.amdhsa_float_denorm_mode_16_64 3
		.amdhsa_dx10_clamp 1
		.amdhsa_ieee_mode 1
		.amdhsa_fp16_overflow 0
		.amdhsa_tg_split 0
		.amdhsa_exception_fp_ieee_invalid_op 0
		.amdhsa_exception_fp_denorm_src 0
		.amdhsa_exception_fp_ieee_div_zero 0
		.amdhsa_exception_fp_ieee_overflow 0
		.amdhsa_exception_fp_ieee_underflow 0
		.amdhsa_exception_fp_ieee_inexact 0
		.amdhsa_exception_int_div_zero 0
	.end_amdhsa_kernel

amdhsa.kernels:
  - .agpr_count:     0
    .args:
      - .actual_access:  read_only
        .address_space:  global
        .offset:         0
        .size:           8
        .value_kind:     global_buffer
      - .actual_access:  read_only
        .address_space:  global
        .offset:         8
        .size:           8
        .value_kind:     global_buffer
      - .actual_access:  read_only
        .address_space:  global
        .offset:         16
        .size:           8
        .value_kind:     global_buffer
      - .actual_access:  write_only
        .address_space:  global
        .offset:         24
        .size:           8
        .value_kind:     global_buffer
      - .actual_access:  write_only
        .address_space:  global
        .offset:         32
        .size:           8
        .value_kind:     global_buffer
      - .actual_access:  write_only
        .address_space:  global
        .offset:         40
        .size:           8
        .value_kind:     global_buffer
    .group_segment_fixed_size: 512
    .kernarg_segment_align: 8
    .kernarg_segment_size: 48
    .language:       OpenCL C
    .language_version:
      - 2
      - 0
    .max_flat_workgroup_size: 1024
    .name:           _Z11prep_kernelPKfS0_S0_PdPtS2_
    .private_segment_fixed_size: 0
    .sgpr_count:     22
    .sgpr_spill_count: 0
    .symbol:         _Z11prep_kernelPKfS0_S0_PdPtS2_.kd
    .uniform_work_group_size: 1
    .uses_dynamic_stack: false
    .vgpr_count:     32
    .vgpr_spill_count: 0
    .wavefront_size: 64
  - .agpr_count:     0
    .args:
      - .actual_access:  read_only
        .address_space:  global
        .offset:         0
        .size:           8
        .value_kind:     global_buffer
      - .actual_access:  read_only
        .address_space:  global
        .offset:         8
        .size:           8
        .value_kind:     global_buffer
      - .actual_access:  read_only
        .address_space:  global
        .offset:         16
        .size:           8
        .value_kind:     global_buffer
      - .actual_access:  read_only
        .address_space:  global
        .offset:         24
        .size:           8
        .value_kind:     global_buffer
      - .actual_access:  read_only
        .address_space:  global
        .offset:         32
        .size:           8
        .value_kind:     global_buffer
      - .actual_access:  read_only
        .address_space:  global
        .offset:         40
        .size:           8
        .value_kind:     global_buffer
      - .actual_access:  write_only
        .address_space:  global
        .offset:         48
        .size:           8
        .value_kind:     global_buffer
      - .actual_access:  write_only
        .address_space:  global
        .offset:         56
        .size:           8
        .value_kind:     global_buffer
      - .actual_access:  write_only
        .address_space:  global
        .offset:         64
        .size:           8
        .value_kind:     global_buffer
    .group_segment_fixed_size: 0
    .kernarg_segment_align: 8
    .kernarg_segment_size: 72
    .language:       OpenCL C
    .language_version:
      - 2
      - 0
    .max_flat_workgroup_size: 512
    .name:           _Z10qkv_kernelPKfS0_S0_PKdPKtS0_PhPfS6_
    .private_segment_fixed_size: 0
    .sgpr_count:     36
    .sgpr_spill_count: 0
    .symbol:         _Z10qkv_kernelPKfS0_S0_PKdPKtS0_PhPfS6_.kd
    .uniform_work_group_size: 1
    .uses_dynamic_stack: false
    .vgpr_count:     192
    .vgpr_spill_count: 0
    .wavefront_size: 64
  - .agpr_count:     16
    .args:
      - .actual_access:  read_only
        .address_space:  global
        .offset:         0
        .size:           8
        .value_kind:     global_buffer
      - .address_space:  global
        .offset:         8
        .size:           8
        .value_kind:     global_buffer
      - .address_space:  global
        .offset:         16
        .size:           8
        .value_kind:     global_buffer
      - .actual_access:  read_only
        .address_space:  global
        .offset:         24
        .size:           8
        .value_kind:     global_buffer
      - .actual_access:  read_only
        .address_space:  global
        .offset:         32
        .size:           8
        .value_kind:     global_buffer
      - .actual_access:  write_only
        .address_space:  global
        .offset:         40
        .size:           8
        .value_kind:     global_buffer
      - .actual_access:  write_only
        .address_space:  global
        .offset:         48
        .size:           8
        .value_kind:     global_buffer
      - .actual_access:  write_only
        .address_space:  global
        .offset:         56
        .size:           8
        .value_kind:     global_buffer
    .group_segment_fixed_size: 0
    .kernarg_segment_align: 8
    .kernarg_segment_size: 64
    .language:       OpenCL C
    .language_version:
      - 2
      - 0
    .max_flat_workgroup_size: 512
    .name:           _Z11attn_kernelPKhS0_S0_PKfS2_PhPfS4_
    .private_segment_fixed_size: 0
    .sgpr_count:     72
    .sgpr_spill_count: 0
    .symbol:         _Z11attn_kernelPKhS0_S0_PKfS2_PhPfS4_.kd
    .uniform_work_group_size: 1
    .uses_dynamic_stack: false
    .vgpr_count:     256
    .vgpr_spill_count: 0
    .wavefront_size: 64
  - .agpr_count:     0
    .args:
      - .actual_access:  read_only
        .address_space:  global
        .offset:         0
        .size:           8
        .value_kind:     global_buffer
      - .actual_access:  read_only
        .address_space:  global
        .offset:         8
        .size:           8
        .value_kind:     global_buffer
      - .actual_access:  read_only
        .address_space:  global
        .offset:         16
        .size:           8
        .value_kind:     global_buffer
      - .actual_access:  read_only
        .address_space:  global
        .offset:         24
        .size:           8
        .value_kind:     global_buffer
      - .actual_access:  read_only
        .address_space:  global
        .offset:         32
        .size:           8
        .value_kind:     global_buffer
      - .actual_access:  read_only
        .address_space:  global
        .offset:         40
        .size:           8
        .value_kind:     global_buffer
      - .actual_access:  write_only
        .address_space:  global
        .offset:         48
        .size:           8
        .value_kind:     global_buffer
    .group_segment_fixed_size: 16640
    .kernarg_segment_align: 8
    .kernarg_segment_size: 56
    .language:       OpenCL C
    .language_version:
      - 2
      - 0
    .max_flat_workgroup_size: 512
    .name:           _Z14outproj_kernelPKhPKfS2_PKtS2_S2_Pf
    .private_segment_fixed_size: 0
    .sgpr_count:     24
    .sgpr_spill_count: 0
    .symbol:         _Z14outproj_kernelPKhPKfS2_PKtS2_S2_Pf.kd
    .uniform_work_group_size: 1
    .uses_dynamic_stack: false
    .vgpr_count:     109
    .vgpr_spill_count: 0
    .wavefront_size: 64
